# slim + P10 processes each XCD's row tiles in descending order (freshest ACT first) for MALL reuse
# baseline (speedup 1.0000x reference)
; #define LAS __attribute__((address_space(3)))
; DI const char* sptr(const char* p) { const unsigned long long v = (unsigned long long)p; const unsigned lo = __builtin_amdgcn_readfirstlane((unsigned)v), hi = __builtin_amdgcn_readfirstlane((unsigned)(v >> 32)); return (const char*)(((unsigned long long)hi << 32) | lo); }
; #define PG8_STAGE_B(bufoff, gbase) do { const char* sb_ = (const char*)(gbase); PG8_GLDS(sb_ + PG8_OPQ(voffB[0]), lds + (bufoff) + ldsw); PG8_GLDS(sb_ + PG8_OPQ(voffB[1]), lds + (bufoff) + ldsw + 8192); } while (0)
; #define PG8_STAGE_A(bufoff, gbase, o0, o1) do { const char* sb_ = (const char*)(gbase); PG8_GLDS(sb_ + PG8_OPQ(o0), lds + (bufoff) + ldsw); PG8_GLDS(sb_ + PG8_OPQ(o1), lds + (bufoff) + ldsw + 8192); } while (0)
; #define PG8_WAIT_V(n) asm volatile("s_waitcnt vmcnt(" #n ")" ::: "memory")
; #define PG8_BAR __builtin_amdgcn_s_barrier()
;     DI bool next(int i, Unit& u) const {
;         const long L = (long)i * G + c; if (L >= nwg) return false;
;         int wgid = (int)L; { const int q = nwg / NXCD, r = nwg % NXCD, xcd = wgid % NXCD, off = wgid / NXCD; wgid = (xcd < r ? xcd * (q + 1) : r * (q + 1) + (xcd - r) * q) + off; }
;         const int nig = WGM * nN, gid = wgid / nig, fm = gid * WGM, gsz = (nM - fm) < WGM ? (nM - fm) : WGM;
;         u.pm = fm + ((wgid % nig) % gsz); u.pn = (wgid % nig) / gsz; u.e = 0; return true;
; template <class Epi, bool GATHER, bool EXPERT, bool FP8>
; DI void gemm_phase(LAS unsigned char* lds, const Gemm g, const StaticOrder& S, const Epi& E) {
;     ...
;     PG8_OFFS(coffA, cur.pm);
;     const char* cA = sptr((const char*)g.A + (GATHER ? (size_t)0 : (size_t)cur.pm * tstep));
;     const char* cB = sptr((const char*)g.Bt + (size_t)cur.e * g.estride + (size_t)cur.pn * tstep);
;     LAS unsigned char* est = g.estash + wid * 768;
;     if (Epi::STASH) E.prefetch(cur, wr, wc, lane, est);
;     LAS unsigned char* stash = g.stash + wid * 256;
;     PG8_STAGE_B(PG8_SB(0, 0), cB); PG8_STAGE_B(PG8_SB(0, 1), cB + hstep); PG8_STAGE_A(PG8_SA(0, 0), cA, coffA[0][0], coffA[0][1]); PG8_STAGE_A(PG8_SA(0, 1), cA, coffA[1][0], coffA[1][1]);
;     if (wr == 1) PG8_BAR;
;     PG8_WAIT_V(2); PG8_BAR;
;     PG8_STAGE_B(PG8_SB(1, 0), cB + kstep); PG8_STAGE_A(PG8_SA(1, 0), cA + kstep, coffA[0][0], coffA[0][1]); PG8_STAGE_B(PG8_SB(1, 1), cB + hstep + kstep);
;     PG8_WAIT_V(6); PG8_BAR;
.LBB0_1149:
	s_cmp_lt_i32 s86, 11
	s_cselect_b64 s[0:1], -1, 0
	s_and_b64 s[0:1], s[0:1], s[2:3]
	s_andn2_b64 vcc, exec, s[0:1]
	s_cbranch_vccnz .LBB0_1168
	s_lshl_b32 s2, s46, 3
	s_cmp_ge_i32 s81, s2
	v_readfirstlane_b32 s3, v0
	s_cbranch_scc1 .LBB0_1168
	s_add_u32 s19, s94, 0x74400000
	s_addc_u32 s40, s95, 0
	s_add_u32 s41, s94, 0x24000000
	s_addc_u32 s42, s95, 0
	v_lshrrev_b32_e32 v3, 1, v0
	v_bfe_u32 v4, v0, 2, 2
	s_add_u32 s0, s94, 0x272b000
	v_and_or_b32 v3, v3, 24, v4
	v_lshrrev_b32_e32 v4, 3, v0
	s_movk_i32 s6, 0x60
	s_addc_u32 s1, s95, 0
	v_and_b32_e32 v6, 32, v4
	v_bitop3_b32 v4, v4, s6, 64 bitop3:0xc8
	s_lshr_b32 s6, s3, 1
	s_ashr_i32 s47, s81, 31
	s_and_b32 s45, s6, 0x60
	s_lshr_b32 s6, s47, 29
	s_add_i32 s6, s81, s6
	s_lshr_b32 s5, s3, 6
	s_lshr_b32 s4, s3, 8
	s_ashr_i32 s7, s6, 3
	s_sub_i32 s7, s46, s7
	s_add_i32 s7, s7, -1
	s_and_b32 s6, s6, -8
	s_lshl_b32 s43, s5, 10
	s_lshl_b32 s44, s4, 6
	s_sub_i32 s6, s81, s6
	s_add_i32 s48, s46, 1
	s_cmp_lt_i32 s6, 0
	s_cselect_b32 s8, s48, s46
	s_mul_i32 s6, s8, s6
	s_add_i32 s6, s6, s7
	s_ashr_i32 s7, s6, 31
	s_lshr_b32 s7, s7, 26
	s_add_i32 s8, s6, s7
	s_ashr_i32 s7, s8, 6
	s_lshl_b32 s9, s7, 3
	s_sub_i32 s7, s46, s9
	v_lshrrev_b32_e32 v7, 5, v0
	s_min_i32 s10, s7, 8
	v_and_b32_e32 v7, 4, v7
	s_abs_i32 s11, s10
	v_or3_b32 v6, v7, v6, v3
	v_or3_b32 v3, v7, v4, v3
	v_cvt_f32_u32_e32 v4, s11
	v_lshlrev_b32_e32 v1, 4, v0
	v_and_b32_e32 v2, 32, v0
	v_bitop3_b32 v2, v1, v2, 48 bitop3:0x6c
	v_and_b32_e32 v5, 64, v0
	v_lshlrev_b32_e32 v6, 11, v6
	v_lshlrev_b32_e32 v3, 11, v3
	v_or3_b32 v150, v6, v5, v2
	v_or3_b32 v151, v3, v5, v2
	v_rcp_iflag_f32_e32 v2, v4
	s_sub_i32 s13, 0, s11
	s_andn2_b32 s8, s8, 63
	s_sub_i32 s6, s6, s8
	v_mul_f32_e32 v2, 0x4f7ffffe, v2
	v_cvt_u32_f32_e32 v2, v2
	s_abs_i32 s12, s6
	s_xor_b32 s8, s6, s10
	s_ashr_i32 s8, s8, 31
	v_readfirstlane_b32 s14, v2
	s_mul_i32 s13, s13, s14
	s_mul_hi_u32 s13, s14, s13
	s_add_i32 s14, s14, s13
	s_mul_hi_u32 s13, s12, s14
	s_mul_i32 s14, s13, s11
	s_sub_i32 s12, s12, s14
	s_add_i32 s14, s13, 1
	s_sub_i32 s15, s12, s11
	s_cmp_ge_u32 s12, s11
	s_cselect_b32 s13, s14, s13
	s_cselect_b32 s12, s15, s12
	s_add_i32 s14, s13, 1
	s_cmp_ge_u32 s12, s11
	s_cselect_b32 s11, s14, s13
	s_xor_b32 s11, s11, s8
	s_sub_i32 s28, s11, s8
	s_mul_i32 s8, s28, s10
	s_sub_i32 s6, s6, s8
	s_add_i32 s30, s9, s6
	s_lshl_b32 s6, s30, 2
	s_add_i32 s6, s6, 0
	s_add_i32 s6, s6, 0x20000
	v_mov_b32_e32 v2, s6
	v_mov_b32_e32 v3, v0
	ds_read_b32 v2, v2
	s_ashr_i32 s31, s30, 31
	v_ashrrev_i32_e32 v5, 31, v3
	v_lshrrev_b32_e32 v5, 26, v5
	v_lshlrev_b32_e32 v4, 4, v3
	v_add_u32_e32 v5, v3, v5
	v_bfe_i32 v3, v3, 27, 1
	v_lshrrev_b32_e32 v3, 22, v3
	v_add_u32_e32 v3, v4, v3
	v_and_b32_e32 v3, 0xfffffc00, v3
	v_sub_u32_e32 v3, v4, v3
	v_lshrrev_b32_e32 v6, 4, v3
	v_bitop3_b32 v3, v6, v3, 32 bitop3:0x6c
	v_ashrrev_i32_e32 v7, 31, v3
	v_lshrrev_b32_e32 v7, 26, v7
	v_ashrrev_i32_e32 v5, 6, v5
	v_add_u32_e32 v7, v3, v7
	v_lshlrev_b32_e32 v6, 3, v5
	v_lshrrev_b32_e32 v8, 6, v7
	v_and_b32_e32 v7, 0xc0, v7
	s_lshl_b64 s[8:9], s[30:31], 19
	v_and_b32_e32 v6, 0x1ffff0, v6
	v_lshlrev_b32_e32 v5, 5, v5
	v_sub_u32_e32 v3, v3, v7
	v_mov_b32_e32 v7, 1
	s_waitcnt lgkmcnt(0)
	v_readfirstlane_b32 s10, v2
	s_add_u32 s34, s19, s8
	v_add_u32_e32 v6, v8, v6
	v_and_b32_e32 v5, 32, v5
	v_ashrrev_i16_sdwa v3, v7, sext(v3) dst_sel:DWORD dst_unused:UNUSED_PAD src0_sel:DWORD src1_sel:BYTE_0
	s_addc_u32 s35, s40, s9
	s_ashr_i32 s11, s10, 31
	v_bfe_i32 v3, v3, 0, 16
	v_lshl_or_b32 v5, v6, 10, v5
	s_lshl_b64 s[8:9], s[10:11], 22
	v_add_lshl_u32 v152, v5, v3, 1
	v_add_u32_e32 v3, 0x2000, v4
	s_add_u32 s6, s41, s8
	v_ashrrev_i32_e32 v4, 31, v3
	s_addc_u32 s12, s42, s9
	s_ashr_i32 s29, s28, 31
	v_lshrrev_b32_e32 v4, 22, v4
	s_lshl_b64 s[8:9], s[28:29], 19
	v_add_u32_e32 v4, v3, v4
	s_add_u32 s36, s6, s8
	v_ashrrev_i32_e32 v4, 10, v4
	s_addc_u32 s37, s12, s9
	s_mulk_i32 s5, 0x300
	s_lshl_b32 s8, s30, 8
	v_mul_i32_i24_e32 v5, 0x400, v4
	s_add_i32 s5, s5, 0
	s_ashr_i32 s9, s8, 31
	v_sub_u32_e32 v3, v3, v5
	s_add_i32 s29, s5, 0x24000
	s_lshl_b64 s[8:9], s[8:9], 2
	v_lshrrev_b32_e32 v5, 4, v3
	s_add_u32 s6, s0, s8
	v_bitop3_b32 v3, v5, v3, 32 bitop3:0x6c
	s_addc_u32 s9, s1, s9
	s_and_b32 s8, s3, 0xffffff00
	v_ashrrev_i32_e32 v6, 31, v3
	s_add_u32 s8, s6, s8
	v_lshrrev_b32_e32 v6, 26, v6
	s_addc_u32 s9, s9, 0
	v_lshlrev_b32_e32 v144, 2, v224
	s_mov_b32 m0, s29
	v_add_u32_e32 v6, v3, v6
	global_load_lds_dword v144, s[8:9]
	s_add_i32 m0, s5, 0x24100
	s_lshl_b64 s[10:11], s[10:11], 13
	v_lshlrev_b32_e32 v5, 3, v4
	v_lshrrev_b32_e32 v8, 6, v6
	v_and_b32_e32 v6, 0xc0, v6
	s_add_u32 s6, s90, s10
	v_and_b32_e32 v5, 0x1ffff0, v5
	v_lshlrev_b32_e32 v4, 5, v4
	v_sub_u32_e32 v3, v3, v6
	s_addc_u32 s12, s91, s11
	s_lshl_b32 s10, s28, 8
	v_add_u32_e32 v5, v8, v5
	v_and_b32_e32 v4, 32, v4
	v_ashrrev_i16_sdwa v3, v7, sext(v3) dst_sel:DWORD dst_unused:UNUSED_PAD src0_sel:DWORD src1_sel:BYTE_0
	s_ashr_i32 s11, s10, 31
	v_bfe_i32 v3, v3, 0, 16
	v_lshl_or_b32 v4, v5, 10, v4
	v_mov_b32_e32 v145, 0
	s_lshl_b64 s[10:11], s[10:11], 2
	v_add_lshl_u32 v154, v4, v3, 1
	v_lshl_add_u64 v[2:3], s[8:9], 0, v[144:145]
	s_mov_b64 s[8:9], 0x200
	s_add_u32 s10, s6, s10
	v_lshl_add_u64 v[2:3], v[2:3], 0, s[8:9]
	s_addc_u32 s11, s12, s11
	v_and_b32_e32 v144, 0x200, v1
	s_mov_b32 s7, 0
	global_load_lds_dword v[2:3], off
	v_lshl_add_u64 v[2:3], s[10:11], 0, v[144:145]
	s_lshl_b32 s6, s45, 2
	v_and_b32_e32 v1, 31, v0
	v_lshl_add_u64 v[2:3], v[2:3], 0, s[6:7]
	v_lshlrev_b32_e32 v144, 2, v1
	v_lshl_add_u64 v[2:3], v[2:3], 0, v[144:145]
	s_add_i32 m0, s5, 0x24200
	v_mov_b32_e32 v1, v150
	s_add_i32 s31, s43, 0
	global_load_lds_dword v[2:3], off
	s_add_i32 m0, s31, 0x10000
	v_add_u32_e32 v153, 0x40000, v152
	global_load_lds_dwordx4 v1, s[36:37]
	v_mov_b32_e32 v1, v151
	s_add_i32 m0, s31, 0x12000
	s_add_u32 s10, s36, 0x40000
	global_load_lds_dwordx4 v1, s[36:37]
	v_mov_b32_e32 v1, v150
	s_addc_u32 s11, s37, 0
	s_add_i32 m0, s31, 0x14000
	s_add_i32 s49, s31, 0x2000
	global_load_lds_dwordx4 v1, s[10:11]
	v_mov_b32_e32 v1, v151
	s_add_i32 m0, s31, 0x16000
	s_add_i32 s50, s31, 0x4000
	global_load_lds_dwordx4 v1, s[10:11]
	v_mov_b32_e32 v1, v152
	s_mov_b32 m0, s31
	v_add_u32_e32 v155, 0x40000, v154
	global_load_lds_dwordx4 v1, s[34:35]
	v_mov_b32_e32 v1, v154
	s_mov_b32 m0, s49
	s_add_i32 s51, s31, 0x6000
	global_load_lds_dwordx4 v1, s[34:35]
	v_mov_b32_e32 v1, v153
	s_mov_b32 m0, s50
	s_cmp_eq_u32 s4, 1
	global_load_lds_dwordx4 v1, s[34:35]
	v_mov_b32_e32 v1, v155
	s_mov_b32 m0, s51
	s_cselect_b64 s[10:11], -1, 0
	global_load_lds_dwordx4 v1, s[34:35]
	s_cmp_lg_u32 s4, 1
	v_lshlrev_b32_e32 v1, 2, v0
	s_cbranch_scc1 .LBB0_1153
	s_barrier

; DI const char* sptr(const char* p) { const unsigned long long v = (unsigned long long)p; const unsigned lo = __builtin_amdgcn_readfirstlane((unsigned)v), hi = __builtin_amdgcn_readfirstlane((unsigned)(v >> 32)); return (const char*)(((unsigned long long)hi << 32) | lo); }
;     DI bool next(int i, Unit& u) const {
;         const long L = (long)i * G + c; if (L >= nwg) return false;
;         int wgid = (int)L; { const int q = nwg / NXCD, r = nwg % NXCD, xcd = wgid % NXCD, off = wgid / NXCD; wgid = (xcd < r ? xcd * (q + 1) : r * (q + 1) + (xcd - r) * q) + off; }
;         const int nig = WGM * nN, gid = wgid / nig, fm = gid * WGM, gsz = (nM - fm) < WGM ? (nM - fm) : WGM;
;         u.pm = fm + ((wgid % nig) % gsz); u.pn = (wgid % nig) / gsz; u.e = 0; return true;
; template <class Epi, bool GATHER, bool EXPERT, bool FP8>
; DI void gemm_phase(LAS unsigned char* lds, const Gemm g, const StaticOrder& S, const Epi& E) {
;     ...
;         const bool has_next = S.next(ui + 1, nxt);
;         if (EXPERT) nxt.e = has_next ? __builtin_amdgcn_readfirstlane(g.tile_e[nxt.pm]) : 0;
;         const char* nA = sptr(has_next ? (const char*)g.A + (GATHER ? (size_t)0 : (size_t)nxt.pm * tstep) : cA);
;         const char* nB = sptr(has_next ? (const char*)g.Bt + (size_t)nxt.e * g.estride + (size_t)nxt.pn * tstep : cB);
.LBB0_1156:
	s_add_i32 s61, s61, 1
	v_readlane_b32 s2, v254, 2
	s_mul_i32 s0, s61, s54
	s_mul_hi_u32 s1, s61, s2
	s_add_i32 s1, s1, s0
	s_mul_i32 s0, s61, s2
	s_add_u32 s0, s0, s81
	s_addc_u32 s1, s1, s47
	v_cmp_ge_i64_e32 vcc, s[0:1], v[146:147]
	v_cmp_lt_i64_e64 s[4:5], s[0:1], v[146:147]
	s_cbranch_vccnz .LBB0_1158
	s_ashr_i32 s1, s0, 31
	s_lshr_b32 s1, s1, 29
	s_add_i32 s1, s0, s1
	s_ashr_i32 s2, s1, 3
	s_sub_i32 s2, s46, s2
	s_add_i32 s2, s2, -1
	s_and_b32 s1, s1, -8
	s_sub_i32 s0, s0, s1
	s_cmp_lt_i32 s0, 0
	s_cselect_b32 s1, s48, s46
	s_mul_i32 s0, s1, s0
	s_add_i32 s0, s0, s2
	s_ashr_i32 s1, s0, 31
	s_lshr_b32 s1, s1, 26
	s_add_i32 s1, s0, s1
	s_ashr_i32 s2, s1, 6
	s_lshl_b32 s2, s2, 3
	s_sub_i32 s3, s46, s2
	s_min_i32 s3, s3, 8
	s_abs_i32 s20, s3
	v_cvt_f32_u32_e32 v0, s20
	s_sub_i32 s22, 0, s20
	s_andn2_b32 s1, s1, 63
	s_sub_i32 s0, s0, s1
	v_rcp_iflag_f32_e32 v0, v0
	s_abs_i32 s1, s0
	s_xor_b32 s21, s0, s3
	s_ashr_i32 s21, s21, 31
	v_mul_f32_e32 v0, 0x4f7ffffe, v0
	v_cvt_u32_f32_e32 v0, v0
	s_nop 0
	v_readfirstlane_b32 s23, v0
	s_mul_i32 s22, s22, s23
	s_mul_hi_u32 s22, s23, s22
	s_add_i32 s23, s23, s22
	s_mul_hi_u32 s22, s1, s23
	s_mul_i32 s23, s22, s20
	s_sub_i32 s1, s1, s23
	s_add_i32 s24, s22, 1
	s_sub_i32 s23, s1, s20
	s_cmp_ge_u32 s1, s20
	s_cselect_b32 s22, s24, s22
	s_cselect_b32 s1, s23, s1
	s_add_i32 s23, s22, 1
	s_cmp_ge_u32 s1, s20
	s_cselect_b32 s1, s23, s22
	s_xor_b32 s1, s1, s21
	s_sub_i32 s20, s1, s21
	s_mul_i32 s1, s20, s3
	s_sub_i32 s0, s0, s1
	s_add_i32 s22, s0, s2
